# speedup vs baseline: 1.0072x; 1.0009x over previous
.LBB1_26:
	s_waitcnt vmcnt(35)
	v_and_b32_e32 v113, 3, v0
	s_and_b32 s18, s2, 15
	v_cmp_eq_u32_e32 vcc, 0, v113
	v_cmp_gt_u32_e64 s[4:5], 12, v92
	s_and_b64 s[12:13], vcc, s[4:5]
	s_lshl_b32 s4, s3, 12
	s_lshl_b32 s5, s18, 8
	s_or_b32 s4, s4, s5
	s_mul_hi_i32 s5, s4, 0x6000
	s_mulk_i32 s4, 0x6000
	s_lshl_b32 s3, s3, 8
	s_add_u32 s16, s24, s4
	s_addc_u32 s17, s25, s5
	s_ashr_i32 s4, s21, 31
	s_lshr_b32 s4, s4, 29
	s_add_i32 s4, s21, s4
	s_ashr_i32 s19, s4, 3
	v_and_b32_e32 v101, 1, v74
	v_lshl_or_b32 v74, v91, 1, v95
	s_min_i32 s4, s19, 0xff
	v_mul_u32_u24_e32 v74, 0x60, v74
	v_lshlrev_b32_e32 v75, 1, v92
	s_mul_hi_i32 s5, s4, 0x6000
	s_mulk_i32 s4, 0x6000
	v_or3_b32 v88, v74, v75, v101
	s_add_u32 s4, s16, s4
	s_addc_u32 s5, s17, s5
	v_lshlrev_b64 v[102:103], 4, v[88:89]
	v_lshl_add_u64 v[104:105], s[4:5], 0, v[102:103]
	global_load_dwordx4 v[82:85], v[104:105], off
	global_load_dwordx4 v[74:77], v[104:105], off offset:512
	global_load_dwordx4 v[78:81], v[104:105], off offset:1024
	s_waitcnt vmcnt(5)
	v_mul_f32_e32 v88, 0xbfb8aa3b, v97
	v_mul_f32_e32 v99, 0x3c91a2b4, v88
	s_waitcnt vmcnt(4)
	v_mul_f32_e32 v88, 0x4038aa3b, v96
	v_mul_f32_e32 v104, 0x3c91a2b4, v88
	v_lshrrev_b32_e32 v88, 2, v92
	v_and_b32_e32 v92, 4, v92
	v_cmp_lt_u32_e64 s[4:5], 1, v93
	v_mov_b32_e32 v93, 0xd0
	v_cmp_ne_u32_e32 vcc, 0, v92
	v_lshlrev_b32_e32 v107, 3, v88
	v_sub_u32_e32 v88, 0, v107
	v_cndmask_b32_e32 v92, 0, v93, vcc
	v_add_u32_e32 v106, v92, v86
	v_and_b32_e32 v92, 12, v0
	v_mul_u32_u24_e32 v86, 0xd0, v101
	v_mad_u32_u24 v91, v91, 24, v92
	v_mul_u32_u24_e32 v93, 12, v95
	v_lshlrev_b32_e32 v92, 20, v101
	v_add3_u32 v112, v91, v86, v93
	v_lshl_or_b32 v86, s18, 21, v90
	v_add3_u32 v86, v86, s3, v92
	v_mul_f32_e32 v1, 0xbfb8aa3b, v1
	v_and_b32_e32 v114, 24, v88
	v_or_b32_e32 v88, v86, v94
	s_min_i32 s3, s19, 0xfe
	v_mul_f32_e32 v1, 0x3c91a2b4, v1
	s_waitcnt vmcnt(3)
	v_mul_f32_e32 v105, 0x4038aa3b, v100
	v_add_u32_e32 v108, 16, v106
	v_add_u32_e32 v109, 0x70, v106
	v_add_u32_e32 v110, 0x1b0, v106
	v_add_u32_e32 v111, 0x210, v106
	v_mul_u32_u24_e32 v113, 6, v113
	s_add_i32 s19, s3, 1
	v_lshl_add_u64 v[100:101], s[16:17], 0, v[102:103]
	v_lshl_add_u64 v[102:103], v[88:89], 1, s[14:15]
	s_sub_i32 s3, 0x7ff, s21
	v_mov_b32_e32 v115, 0x7f7f7f7f
	s_mov_b32 s16, 0x42700000
	s_mov_b32 s17, 0x41f00000
	s_mov_b32 s18, 0x41700000
	v_mov_b32_e32 v116, 0x6000
	v_mov_b32_e32 v117, 0x4b400000
	v_mov_b32_e32 v118, 0x4b400008
	v_mov_b32_e32 v119, 0x4b400010
	v_mbcnt_lo_u32_b32 v200, -1, 0
	v_mbcnt_hi_u32_b32 v200, -1, v200
	v_and_b32_e32 v201, 3, v200
	v_and_b32_e32 v202, 15, v200
	v_cmp_gt_u32_e32 vcc, 8, v202
	s_nop 1
	v_cndmask_b32_e64 v178, 0, v115, vcc
	v_cndmask_b32_e64 v179, v115, 0, vcc
	v_lshlrev_b32_e32 v181, 1, v201
	v_sub_u32_e32 v202, 22, v181
	v_lshlrev_b32_e64 v180, v202, 1
	v_sub_u32_e32 v202, 16, v181
	v_lshlrev_b32_e64 v181, v202, 1
	v_readfirstlane_b32 s51, v112
	v_lshrrev_b32_e32 v202, 4, v200
	v_lshlrev_b32_e32 v192, 5, v202
	v_bfe_u32 v202, v200, 2, 1
	v_mul_u32_u24_e32 v202, 0x110, v202
	v_add_u32_e32 v192, v192, v202
	s_mul_i32 s46, s51, 0xaaab
	s_lshr_b32 s46, s46, 15
	v_bfe_u32 v202, v200, 4, 1
	v_mul_u32_u24_e32 v184, 0x110, v202
	v_lshrrev_b32_e32 v202, 5, v200
	v_mul_u32_u24_e32 v202, 12, v202
	v_add_u32_e32 v184, v184, v202
	v_bfe_u32 v202, v200, 2, 2
	v_mul_u32_u24_e32 v164, 3, v202
	v_add3_u32 v184, v184, v164, v201
	v_add_u32_e32 v184, s46, v184
	v_add_u32_e32 v202, 0x100, v202
	v_lshrrev_b32_e32 v164, 4, v200
	v_and_b32_e32 v165, 1, v164
	v_mul_u32_u24_e32 v165, 0x110, v165
	v_lshrrev_b32_e32 v164, 1, v164
	v_lshl_add_u32 v165, v164, 2, v165
	v_add_u32_e32 v202, v202, v165
	v_cmp_eq_u32_e32 vcc, 3, v201
	s_nop 1
	v_cndmask_b32_e32 v184, v184, v202, vcc
	v_subrev_u32_e32 v185, s14, v102
	s_mov_b32 s44, s21
	s_mov_b32 s45, s22
	s_lshr_b32 s46, s44, 3
	s_add_i32 s46, s46, 1
	s_mul_i32 s46, s46, 0x6000
	s_mov_b32 s47, 0
	v_lshl_add_u64 v[196:197], v[100:101], 0, s[46:47]
	s_mov_b32 s42, 0x6000
	s_mov_b32 s43, 0
	s_sub_i32 s46, s44, 1
	s_sub_i32 s47, 0x800, s44
	s_and_b64 s[40:41], s[6:7], exec
	s_cselect_b32 s46, s46, s47
	s_cselect_b32 s41, 0, -1
	s_xor_b32 s40, s41, 0x400
	s_sub_i32 s40, s40, s41
	s_ashr_i32 s47, s46, 31
	s_lshl_b64 s[46:47], s[46:47], 10
	s_add_u32 s48, s14, s46
	s_addc_u32 s49, s15, s47
	s_waitcnt vmcnt(0) lgkmcnt(0)
	v_mov_b32_e32 v176, v87
	v_add_f32_e32 v169, -1.0, v87
	v_rcp_f32_e32 v186, v104
	s_nop 1
	v_mul_f32_e32 v188, v105, v186
	v_mov_b32_e32 v189, 0
	v_mov_b32_e32 v190, 0
	v_mov_b32_e32 v191, 0
	s_nop 1
	s_cmp_lt_i32 s44, s45
	s_cbranch_scc0 .Lscan_exit_st
	ds_read_b128 v[122:125], v192
	ds_read_b64 v[126:127], v192 offset:16
	s_waitcnt lgkmcnt(0)
	s_cmp_lt_u32 s51, 96
	s_cbranch_scc0 .Lscan_entry_b_st
	s_branch .Lscan_enter_a_st
	.p2align 6

.LBB2_12:
	s_or_b64 exec, exec, s[0:1]
	v_and_b32_e32 v97, 1, v74
	v_mov_b32_e32 v74, s8
	v_mov_b32_e32 v75, s9
	v_lshl_or_b32 v76, s2, 9, v0
	v_mov_b32_e32 v77, v87
	v_lshl_add_u64 v[74:75], v[76:77], 2, v[74:75]
	s_waitcnt lgkmcnt(0)
	s_barrier
	global_load_dword v118, v[74:75], off
	v_and_b32_e32 v74, 4, v90
	v_mov_b32_e32 v75, 0xd0
	v_cmp_ne_u32_e32 vcc, 0, v74
	v_and_b32_e32 v110, 3, v0
	v_cmp_gt_u32_e64 s[0:1], 12, v90
	v_cndmask_b32_e32 v74, 0, v75, vcc
	v_cmp_eq_u32_e32 vcc, 0, v110
	s_and_b64 s[4:5], vcc, s[0:1]
	s_lshl_b32 s1, s2, 21
	v_add_u32_e32 v109, v74, v86
	s_mul_i32 s0, s2, 0x600000
	v_lshl_or_b32 v74, v89, 1, v88
	s_and_b32 s2, s1, 0x1e00000
	v_mul_u32_u24_e32 v74, 0x60, v74
	v_lshlrev_b32_e32 v75, 1, v90
	s_add_u32 s0, s14, s0
	s_addc_u32 s1, s15, 0
	v_or3_b32 v86, v74, v75, v97
	v_lshl_add_u64 v[98:99], v[86:87], 4, s[0:1]
	s_mov_b64 s[0:1], 0x5a0000
	v_lshl_add_u64 v[100:101], v[98:99], 0, s[0:1]
	s_mov_b32 s0, 0x5a0000
	v_add_co_u32_e32 v102, vcc, s0, v98
	s_waitcnt vmcnt(4)
	v_mul_f32_e32 v86, 0xbfb8aa3b, v95
	v_addc_co_u32_e32 v103, vcc, 0, v99, vcc
	global_load_dwordx4 v[82:85], v[102:103], off
	global_load_dwordx4 v[74:77], v[100:101], off offset:512
	global_load_dwordx4 v[78:81], v[100:101], off offset:1024
	v_mul_f32_e32 v100, 0x3c91a2b4, v86
	s_waitcnt vmcnt(6)
	v_mul_f32_e32 v86, 0xbfb8aa3b, v94
	v_mul_f32_e32 v101, 0x3c91a2b4, v86
	s_waitcnt vmcnt(5)
	v_mul_f32_e32 v86, 0x4038aa3b, v93
	v_and_b32_e32 v0, 12, v0
	v_mul_f32_e32 v102, 0x3c91a2b4, v86
	v_lshrrev_b32_e32 v86, 2, v90
	v_mul_u32_u24_e32 v90, 0xd0, v97
	v_mad_u32_u24 v0, v89, 24, v0
	v_mul_u32_u24_e32 v88, 12, v88
	v_add3_u32 v93, v0, v90, v88
	v_or_b32_e32 v0, s2, v1
	v_lshlrev_b32_e32 v104, 3, v86
	v_lshlrev_b32_e32 v89, 20, v97
	v_lshl_add_u32 v0, s22, 8, v0
	v_sub_u32_e32 v86, 0, v104
	v_or3_b32 v0, v0, v89, v92
	v_and_b32_e32 v111, 24, v86
	v_lshlrev_b32_e32 v86, 1, v0
	s_mov_b64 s[6:7], 0x5a6000
	v_lshl_add_u64 v[0:1], s[12:13], 0, v[86:87]
	v_lshl_add_u64 v[86:87], v[98:99], 0, s[6:7]
	s_mov_b64 s[6:7], 0x5a6200
	v_lshl_add_u64 v[88:89], v[98:99], 0, s[6:7]
	s_mov_b64 s[6:7], 0x5a6400
	v_cmp_lt_u32_e64 s[0:1], 1, v91
	s_waitcnt vmcnt(4)
	v_mul_f32_e32 v103, 0x4038aa3b, v96
	s_mov_b32 s3, 0
	v_or_b32_e32 v105, 0x1c400, v109
	v_add_u32_e32 v106, 0x1c410, v109
	v_add_u32_e32 v107, 0x1c470, v109
	v_add_u32_e32 v108, 0x1c5b0, v109
	v_add_u32_e32 v109, 0x1c610, v109
	v_mul_u32_u24_e32 v110, 6, v110
	v_lshl_add_u64 v[90:91], v[98:99], 0, s[6:7]
	s_movk_i32 s22, 0x780
	s_movk_i32 s14, 0x7f
	s_movk_i32 s15, 0xf0
	v_mov_b32_e32 v112, 0x7f7f7f7f
	s_mov_b32 s17, 0x42700000
	s_mov_b32 s18, 0x41f00000
	s_mov_b32 s19, 0x41700000
	s_mov_b64 s[6:7], 0x12000
	s_mov_b64 s[8:9], 0x12200
	s_mov_b64 s[10:11], 0x12400
	v_mov_b32_e32 v113, 0x4b400000
	v_mov_b32_e32 v114, 0x4b400008
	v_mov_b32_e32 v115, 0x4b400010
	v_add_u32_e32 v116, 0x1c5a0, v93
	v_add_u32_e32 v117, 0x1c400, v93
	v_mbcnt_lo_u32_b32 v200, -1, 0
	v_mbcnt_hi_u32_b32 v200, -1, v200
	v_and_b32_e32 v201, 3, v200
	v_and_b32_e32 v202, 15, v200
	v_cmp_gt_u32_e32 vcc, 8, v202
	s_nop 1
	v_cndmask_b32_e64 v178, 0, v112, vcc
	v_cndmask_b32_e64 v179, v112, 0, vcc
	v_lshlrev_b32_e32 v181, 1, v201
	v_sub_u32_e32 v202, 22, v181
	v_lshlrev_b32_e64 v180, v202, 1
	v_sub_u32_e32 v202, 16, v181
	v_lshlrev_b32_e64 v181, v202, 1
	v_readfirstlane_b32 s51, v117
	v_lshrrev_b32_e32 v202, 4, v200
	v_lshlrev_b32_e32 v192, 5, v202
	v_bfe_u32 v202, v200, 2, 1
	v_mul_u32_u24_e32 v202, 0x110, v202
	v_add_u32_e32 v192, v192, v202
	v_add_u32_e32 v192, 0x1c400, v192
	s_sub_u32 s51, s51, 0x1c400
	s_mul_i32 s46, s51, 0xaaab
	s_lshr_b32 s46, s46, 15
	v_bfe_u32 v202, v200, 4, 1
	v_mul_u32_u24_e32 v184, 0x110, v202
	v_lshrrev_b32_e32 v202, 5, v200
	v_mul_u32_u24_e32 v202, 12, v202
	v_add_u32_e32 v184, v184, v202
	v_bfe_u32 v202, v200, 2, 2
	v_mul_u32_u24_e32 v164, 3, v202
	v_add3_u32 v184, v184, v164, v201
	v_add_u32_e32 v184, s46, v184
	v_add_u32_e32 v202, 0x1c500, v202
	v_lshrrev_b32_e32 v164, 4, v200
	v_and_b32_e32 v165, 1, v164
	v_mul_u32_u24_e32 v165, 0x110, v165
	v_lshrrev_b32_e32 v164, 1, v164
	v_lshl_add_u32 v165, v164, 2, v165
	v_add_u32_e32 v202, v202, v165
	v_add_u32_e32 v184, 0x1c400, v184
	v_cmp_eq_u32_e32 vcc, 3, v201
	s_nop 1
	v_cndmask_b32_e32 v184, v184, v202, vcc
	v_subrev_u32_e32 v185, s12, v0
	s_movk_i32 s44, 0x780
	s_movk_i32 s45, 0x800
	s_lshr_b32 s46, s44, 3
	s_add_i32 s46, s46, 1
	s_mul_i32 s46, s46, 0x6000
	s_mov_b32 s47, 0
	v_lshl_add_u64 v[196:197], v[98:99], 0, s[46:47]
	s_mov_b32 s42, 0x6000
	s_mov_b32 s43, 0
	s_sub_i32 s46, s44, 1
	s_sub_i32 s47, 0x800, s44
	s_and_b64 s[40:41], s[20:21], exec
	s_cselect_b32 s46, s46, s47
	s_cselect_b32 s41, 0, -1
	s_xor_b32 s40, s41, 0x400
	s_sub_i32 s40, s40, s41
	s_ashr_i32 s47, s46, 31
	s_lshl_b64 s[46:47], s[46:47], 10
	s_add_u32 s48, s12, s46
	s_addc_u32 s49, s13, s47
	s_waitcnt vmcnt(0) lgkmcnt(0)
	v_mov_b32_e32 v176, v118
	v_add_f32_e32 v169, -1.0, v118
	v_rcp_f32_e32 v186, v102
	s_nop 1
	v_mul_f32_e32 v188, v103, v186
	v_mov_b32_e32 v189, 0
	v_mov_b32_e32 v190, 0
	v_mov_b32_e32 v191, 0
	s_nop 1
	s_cmp_lt_i32 s44, s45
	s_cbranch_scc0 .Lscan_exit_f2
	ds_read_b128 v[122:125], v192
	ds_read_b64 v[126:127], v192 offset:16
	s_waitcnt lgkmcnt(0)
	s_cmp_lt_u32 s51, 96
	s_cbranch_scc0 .Lscan_entry_b_f2
	s_branch .Lscan_enter_a_f2
	.p2align 6
